# k_iter first: 16-B table stores written through (sc1) so the end-of-kernel release has nothing dirty to flush
# speedup vs baseline: 1.0579x; 1.0075x over previous
_Z6k_iterILb1ELb0EEvPKfS1_PKiPK15HIP_vector_typeIfLj4EES7_S1_S1_S3_S1_PfS8_S1_S3_PDF16_PS5_SA_PiSA_SB_:
	s_load_dwordx2 s[4:5], s[0:1], 0x78
	s_load_dwordx8 s[20:27], s[0:1], 0x20
	s_load_dwordx2 s[92:93], s[0:1], 0x18
	v_readfirstlane_b32 s54, v0
	v_cmp_gt_u32_e64 s[8:9], 64, v0
	v_lshlrev_b32_e32 v46, 2, v0
	s_and_saveexec_b64 s[6:7], s[8:9]
	v_mov_b32_e32 v1, 0
	ds_write_b32 v46, v1 offset:29728
	s_or_b64 exec, exec, s[6:7]
	s_lshl_b32 s3, s2, 5
	s_and_b32 s3, s3, 0xe0
	s_lshr_b32 s2, s2, 3
	s_add_i32 s46, s3, s2
	s_lshr_b32 s12, s46, 6
	s_lshl_b32 s13, s46, 6
	s_mov_b32 s47, 0
	s_and_b32 s33, s13, 0xfc0
	s_lshl_b32 s58, s12, 12
	s_lshl_b64 s[2:3], s[46:47], 4
	s_waitcnt lgkmcnt(0)
	s_add_u32 s6, s20, s2
	v_and_b32_e32 v25, 31, v0
	s_addc_u32 s7, s21, s3
	s_or_b32 s59, s58, s33
	v_or_b32_e32 v6, s59, v25
	v_mov_b32_e32 v7, 0
	v_lshlrev_b64 v[2:3], 2, v[6:7]
	v_lshl_add_u64 v[4:5], s[22:23], 0, v[2:3]
	v_lshl_add_u64 v[8:9], s[24:25], 0, v[2:3]
	v_lshl_add_u64 v[2:3], s[26:27], 0, v[2:3]
	global_load_dword v196, v[4:5], off offset:128
	global_load_dword v197, v[8:9], off offset:128
	global_load_dword v198, v[2:3], off offset:128
	global_load_dword v4, v[4:5], off
	global_load_dword v5, v[8:9], off
	global_load_dword v6, v[2:3], off
	s_lshl_b32 s94, s12, 13
	s_add_u32 s94, s92, s94
	s_addc_u32 s95, s93, 0
	v_lshlrev_b32_e32 v199, 4, v0
	global_load_dwordx4 v[192:195], v199, s[94:95]
	s_load_dwordx4 s[36:39], s[6:7], 0x0
	s_bfe_u32 s14, s54, 0x10006
	s_cmpk_lt_u32 s54, 0x80
	s_cselect_b64 s[6:7], -1, 0
	s_waitcnt lgkmcnt(0)
	v_mov_b64_e32 v[2:3], s[38:39]
	v_pk_add_f32 v[2:3], s[36:37], v[2:3]
	s_cmp_eq_u32 s14, 0
	v_pk_mul_f32 v[22:23], v[2:3], 0.5 op_sel_hi:[1,0]
	v_and_b32_e32 v44, 63, v0
	s_cselect_b64 s[10:11], -1, 0
	v_mov_b32_e32 v1, 0xff800000
	v_cmp_gt_u32_e64 s[18:19], 32, v44
	s_and_b64 s[10:11], s[10:11], s[6:7]
	s_and_b64 s[16:17], s[10:11], s[18:19]
	v_lshlrev_b32_e32 v10, 4, v25
	s_waitcnt vmcnt(2)
	v_pk_fma_f32 v[36:37], v[2:3], 0.5, v[4:5] op_sel_hi:[1,0,1] neg_lo:[1,0,0] neg_hi:[1,0,0]
	s_nop 0
	v_pk_mul_f32 v[2:3], v[36:37], v[36:37]
	s_waitcnt vmcnt(1)
	v_cmp_ne_u32_e32 vcc, 0, v6
	v_add_f32_e32 v2, v2, v3
	v_sub_f32_e32 v2, 0x3d23d70a, v2
	v_mul_f32_e32 v2, 0x431044f5, v2
	v_cndmask_b32_e32 v4, v1, v2, vcc
	s_and_saveexec_b64 s[10:11], s[16:17]
	s_cbranch_execz .LBB2_4
	s_mov_b32 s16, 0x439044f5
	v_or_b32_e32 v6, s13, v25
	v_pk_mul_f32 v[2:3], v[36:37], s[16:17] op_sel_hi:[1,0]
	v_mov_b32_e32 v5, v7
	v_lshl_add_u64 v[8:9], v[6:7], 4, s[4:5]
	ds_write_b128 v10, v[2:5] offset:26656
	global_store_dwordx4 v[8:9], v[2:5], off sc1
.LBB2_4:
	s_or_b64 exec, exec, s[10:11]
	s_cmp_lg_u32 s14, 0
	s_cselect_b64 s[10:11], -1, 0
	s_and_b64 s[6:7], s[10:11], s[6:7]
	s_and_b64 s[10:11], s[6:7], s[18:19]
	v_pk_add_f32 v[2:3], v[196:197], v[22:23] neg_lo:[0,1] neg_hi:[0,1]
	s_nop 0
	v_pk_mul_f32 v[6:7], v[2:3], v[2:3]
	v_cmp_ne_u32_e32 vcc, 0, v198
	v_add_f32_e32 v6, v6, v7
	v_sub_f32_e32 v6, 0x3d23d70a, v6
	v_mul_f32_e32 v6, 0x431044f5, v6
	v_cndmask_b32_e32 v8, v1, v6, vcc
	s_and_saveexec_b64 s[6:7], s[10:11]
	s_cbranch_execz .LBB2_6
	s_mov_b32 s10, 0x439044f5
	v_pk_mul_f32 v[6:7], v[2:3], s[10:11] op_sel_hi:[1,0]
	v_mov_b32_e32 v9, 0
	ds_write_b128 v10, v[6:9] offset:27168
	v_add_u32_e32 v10, s13, v25
	v_mov_b32_e32 v11, v9
	v_lshl_add_u64 v[10:11], v[10:11], 4, s[4:5]
	global_store_dwordx4 v[10:11], v[6:9], off offset:512 sc1

.LBB2_13:
	v_add_u32_e32 v10, s61, v0
	v_cmp_gt_i32_e64 s[20:21], s60, v10
	v_add_u32_e32 v10, 0x200, v10
	v_cmp_gt_i32_e64 s[22:23], s60, v10
	v_add_u32_e32 v11, 64, v9
	s_nop 1
	v_cndmask_b32_e64 v10, 0, v11, s[22:23]
	v_lshlrev_b32_e32 v10, 2, v10
	ds_read_b32 v10, v10 offset:24576
	s_waitcnt vmcnt(0)
	v_mov_b32_e32 v14, v184
	v_mov_b32_e32 v15, v185
	v_mov_b32_e32 v12, v186
	v_mov_b32_e32 v13, v187
	s_waitcnt lgkmcnt(0)
	v_lshl_or_b32 v187, v10, 3, v5
	v_add_u32_e32 v10, s58, v187
	v_ashrrev_i32_e32 v11, 31, v10
	v_lshlrev_b64 v[10:11], 2, v[10:11]
	v_lshl_add_u64 v[16:17], s[40:41], 0, v[10:11]
	v_lshl_add_u64 v[18:19], s[42:43], 0, v[10:11]
	v_lshl_add_u64 v[10:11], s[52:53], 0, v[10:11]
	global_load_dword v184, v[16:17], off
	global_load_dword v185, v[18:19], off
	global_load_dword v186, v[10:11], off
	v_pk_add_f32 v[10:11], v[14:15], v[22:23] neg_lo:[0,1] neg_hi:[0,1]
	s_nop 0
	v_pk_mul_f32 v[16:17], v[10:11], v[10:11]
	v_cmp_ne_u32_e64 s[22:23], 0, v12
	v_add_f32_e32 v12, v16, v17
	v_mul_f32_e32 v12, 0xc31044f5, v12
	s_and_saveexec_b64 s[24:25], s[20:21]
	s_cbranch_execz .LBB2_15
	v_cndmask_b32_e64 v18, v30, v12, s[22:23]
	v_mov_b32_e32 v16, v10
	v_mov_b32_e32 v17, v11
	v_mov_b32_e32 v19, v13
	global_store_dwordx4 v[26:27], v[16:19], off offset:-8 sc1
.LBB2_15:
	s_or_b64 exec, exec, s[24:25]
	s_nop 0
	v_sub_f32_e32 v16, s36, v14
	v_subrev_f32_e32 v14, s38, v14
	v_max3_f32 v14, v16, v14, 0
	v_sub_f32_e32 v16, s37, v15
	v_subrev_f32_e32 v15, s39, v15
	v_max3_f32 v15, v16, v15, 0
	v_pk_mul_f32 v[14:15], v[14:15], v[14:15]
	s_nop 0
	v_add_f32_e32 v14, v14, v15
	v_cmp_gt_f32_e64 s[24:25], s62, v14
	s_and_b64 s[22:23], s[22:23], s[24:25]
	s_and_b64 s[24:25], s[20:21], s[22:23]
	v_cndmask_b32_e64 v14, 0, 1, s[24:25]
	v_cmp_ne_u32_e64 s[20:21], 0, v14
	s_and_saveexec_b64 s[22:23], vcc
	s_bcnt1_i32_b64 s64, s[20:21]
	v_mov_b32_e32 v14, s47
	v_mov_b32_e32 v15, s64
	ds_write_b32 v14, v15 offset:2048
	s_or_b64 exec, exec, s[22:23]
	s_waitcnt lgkmcnt(0)
	s_barrier
	ds_read_b128 v[18:21], v7 offset:26624
	ds_read_b128 v[14:17], v7 offset:26640
	s_and_saveexec_b64 s[22:23], s[24:25]
	s_cbranch_execz .LBB2_12
	s_waitcnt lgkmcnt(1)
	v_cndmask_b32_e64 v38, v18, 0, s[54:55]
	v_cndmask_b32_e64 v35, 0, v19, s[16:17]
	v_add_u32_e32 v38, v38, v6
	v_cndmask_b32_e64 v34, 0, v20, s[14:15]
	v_add_u32_e32 v35, v35, v38
	v_cndmask_b32_e64 v33, 0, v21, s[12:13]
	v_add_u32_e32 v34, v34, v35
	s_waitcnt lgkmcnt(0)
	v_cndmask_b32_e64 v32, 0, v14, s[10:11]
	v_add_u32_e32 v33, v33, v34
	v_cndmask_b32_e64 v31, 0, v15, s[6:7]
	v_add_u32_e32 v32, v32, v33
	v_cndmask_b32_e64 v29, 0, v16, s[4:5]
	v_add_u32_e32 v31, v31, v32
	v_cndmask_b32_e64 v28, 0, v17, s[2:3]
	v_add_u32_e32 v29, v29, v31
	v_and_b32_e32 v31, s20, v24
	v_add_u32_e32 v28, v28, v29
	v_and_b32_e32 v29, s21, v1
	v_bcnt_u32_b32 v31, v31, 0
	v_bcnt_u32_b32 v29, v29, v31
	v_add_u32_e32 v28, v28, v29
	v_ashrrev_i32_e32 v29, 31, v28
	v_lshl_add_u64 v[32:33], v[28:29], 4, s[44:45]
	v_cmp_gt_i32_e64 s[20:21], s63, v28
	global_store_dwordx4 v[32:33], v[10:13], off sc1
	s_and_b64 exec, exec, s[20:21]
	s_cbranch_execz .LBB2_12
	v_lshlrev_b32_e32 v28, 4, v28
	ds_write_b128 v28, v[10:13]
	s_branch .LBB2_12

.LBB2_99:
	s_or_b64 exec, exec, s[22:23]
	s_lshr_b32 s66, s33, 3
	s_or_b32 s66, s66, s26
	s_add_i32 s66, s66, s27
	s_mov_b32 s67, 0
	s_lshl_b64 s[66:67], s[66:67], 10
	s_add_u32 s66, s30, s66
	s_addc_u32 s67, s31, s67
	v_lshlrev_b32_e32 v208, 4, v44
	s_waitcnt vmcnt(0)
	v_cvt_pk_f16_f32 v210, v200, v201
	v_cvt_pk_f16_f32 v211, v202, v203
	v_cvt_pk_f16_f32 v212, v204, v205
	v_cvt_pk_f16_f32 v213, v206, v207
	global_store_dwordx4 v208, v[210:213], s[66:67] sc1
	s_getpc_b64 s[66:67]
